# routed gate|up GEMM: L2 software prefetch of f32 weight K-tiles (one 4B/lane LDS-DMA touch per wave and K-tile, two tiles ahead of the register prefetch)
# baseline (speedup 1.0000x reference)
; #define PG8_BWAIT(n) asm volatile("s_waitcnt vmcnt(" #n ")" : "+v"(bv[0]), "+v"(bv[1]), "+v"(bv[2]), "+v"(bv[3]), "+v"(bv[4]), "+v"(bv[5]), "+v"(bv[6]), "+v"(bv[7]) :: "memory")
; #define PG8_STAGE_A(bufoff, V0, V1, kb) do { \
;         __builtin_amdgcn_global_load_lds((const unsigned*)((Abase + (kb)) + (V0)), (LAS unsigned*)(lds + (bufoff) + ldsw), 16, 0, 0); \
;         __builtin_amdgcn_global_load_lds((const unsigned*)((Abase + (kb)) + (V1)), (LAS unsigned*)(lds + (bufoff) + ldsw + 8192), 16, 0, 0); } while (0)
; #define PG8_LDA(dst, b, h) do { _Pragma("unroll") for (int m = 0; m < 4; ++m) _Pragma("unroll") for (int k = 0; k < 2; ++k) dst[m][k] = *(const LAS bf16x8*)(lds + PG8_SA(b, h) + aoff + m * 2048 + k * 1024); } while (0)
; #define PG8_LDB(dst, b, h) do { _Pragma("unroll") for (int n = 0; n < 2; ++n) _Pragma("unroll") for (int k = 0; k < 2; ++k) dst[n][k] = *(const LAS bf16x8*)(lds + PG8_SB(b, h) + boff + n * 2048 + k * 1024); } while (0)
; #define PG8_MMA(ai, bj, At, Bt) do { __builtin_amdgcn_s_setprio(1); _Pragma("unroll") for (int m = 0; m < 4; ++m) _Pragma("unroll") for (int n = 0; n < 2; ++n) _Pragma("unroll") for (int k = 0; k < 2; ++k) \
;         acc[ai][bj][m][n] = __builtin_amdgcn_mfma_f32_16x16x32_bf16(Bt[n][k], At[m][k], acc[ai][bj][m][n], 0, 0, 0); __builtin_amdgcn_s_setprio(0); } while (0)
; #define PG8_WAIT_V(n) asm volatile("s_waitcnt vmcnt(" #n ")" ::: "memory")
; #define PG8_WAIT_L(n) asm volatile("s_waitcnt lgkmcnt(" #n ")" ::: "memory")
; #define PG8_BAR __builtin_amdgcn_s_barrier()
; #define PG8_SCHED __builtin_amdgcn_sched_barrier(0)
; template <class Epi, class Sched, bool ALIGN_EPI>
; __device__ __forceinline__ void gemm_phase(LAS unsigned char* lds, const Gemm g, const Sched& S, const Epi& E) {
;     ...
;             PG8_LDB(B0, 0, 0); PG8_LDB(B1, 0, 1); PG8_SCHED; PG8_LDA(At, 0, 0); PG8_STAGE_A(PG8_SA(1, 1), vc10, vc11, kb1);
;             PG8_WAIT_V(12); PG8_WAIT_L(0); PG8_BAR; PG8_MMA(0, 0, At, B0); PG8_MMA(0, 1, At, B1); PG8_BAR; PG8_SCHED;
;             if (last) { vc10 = vn10; vc11 = vn11; }
;             PG8_BWAIT(2); PG8_BCOMMIT(0); PG8_SCHED; PG8_LDA(At, 0, 1); PG8_BISSUE(t + 3 >= nt ? pbn + (size_t)(t + 3 - nt) * 64 * Sched::LDN : pbc + (size_t)(t + 3) * 64 * Sched::LDN); PG8_STAGE_A(PG8_SA(0, 0), vc00, vc01, kb2);
.LBB0_2251:
	v_add_u32_e32 v162, 0x10000, v240
	v_add_u32_e32 v174, 0x14000, v240
	ds_read_b128 v[178:181], v162
	ds_read_b128 v[182:185], v162 offset:1024
	ds_read_b128 v[186:189], v162 offset:2048
	ds_read_b128 v[190:193], v162 offset:3072
	ds_read_b128 v[162:165], v174
	ds_read_b128 v[166:169], v174 offset:1024
	ds_read_b128 v[170:173], v174 offset:2048
	ds_read_b128 v[174:177], v174 offset:3072
	s_add_i32 s54, s53, 2
	s_add_i32 m0, s40, 0xc000
	s_add_u32 s4, s90, s22
	s_addc_u32 s5, s91, s23
	s_waitcnt lgkmcnt(0)
	ds_read_b128 v[194:197], v241
	ds_read_b128 v[198:201], v241 offset:1024
	ds_read_b128 v[202:205], v241 offset:2048
	ds_read_b128 v[206:209], v241 offset:3072
	ds_read_b128 v[210:213], v241 offset:4096
	ds_read_b128 v[214:217], v241 offset:5120
	ds_read_b128 v[218:221], v241 offset:6144
	ds_read_b128 v[222:225], v241 offset:7168
	global_load_lds_dwordx4 v234, s[4:5]
	s_add_i32 m0, s40, 0xe000
	s_nop 0
	global_load_lds_dwordx4 v235, s[4:5]
	s_waitcnt vmcnt(12)
	s_waitcnt lgkmcnt(0)
	s_barrier
	s_setprio 1
	s_waitcnt lgkmcnt(0)
	v_mfma_f32_16x16x32_bf16 v[158:161], v[178:181], v[194:197], v[158:161]
	v_mfma_f32_16x16x32_bf16 v[150:153], v[186:189], v[194:197], v[150:153]
	v_mfma_f32_16x16x32_bf16 v[142:145], v[178:181], v[202:205], v[142:145]
	v_mfma_f32_16x16x32_bf16 v[134:137], v[186:189], v[202:205], v[134:137]
	v_mfma_f32_16x16x32_bf16 v[126:129], v[178:181], v[210:213], v[126:129]
	v_mfma_f32_16x16x32_bf16 v[118:121], v[186:189], v[210:213], v[118:121]
	v_mfma_f32_16x16x32_bf16 v[110:113], v[178:181], v[218:221], v[110:113]
	v_mfma_f32_16x16x32_bf16 v[102:105], v[186:189], v[218:221], v[102:105]
	v_mfma_f32_16x16x32_bf16 v[158:161], v[182:185], v[198:201], v[158:161]
	v_mfma_f32_16x16x32_bf16 v[150:153], v[190:193], v[198:201], v[150:153]
	v_mfma_f32_16x16x32_bf16 v[142:145], v[182:185], v[206:209], v[142:145]
	v_mfma_f32_16x16x32_bf16 v[134:137], v[190:193], v[206:209], v[134:137]
	v_mfma_f32_16x16x32_bf16 v[126:129], v[182:185], v[214:217], v[126:129]
	v_mfma_f32_16x16x32_bf16 v[118:121], v[190:193], v[214:217], v[118:121]
	v_mfma_f32_16x16x32_bf16 v[110:113], v[182:185], v[222:225], v[110:113]
	v_mfma_f32_16x16x32_bf16 v[102:105], v[190:193], v[222:225], v[102:105]
	s_setprio 0
	s_setprio 1
	v_mfma_f32_16x16x32_bf16 v[154:157], v[162:165], v[194:197], v[154:157]
	v_mfma_f32_16x16x32_bf16 v[146:149], v[170:173], v[194:197], v[146:149]
	v_mfma_f32_16x16x32_bf16 v[138:141], v[162:165], v[202:205], v[138:141]
	v_mfma_f32_16x16x32_bf16 v[130:133], v[170:173], v[202:205], v[130:133]
	v_mfma_f32_16x16x32_bf16 v[122:125], v[162:165], v[210:213], v[122:125]
	v_mfma_f32_16x16x32_bf16 v[114:117], v[170:173], v[210:213], v[114:117]
	v_mfma_f32_16x16x32_bf16 v[106:109], v[162:165], v[218:221], v[106:109]
	v_mfma_f32_16x16x32_bf16 v[98:101], v[170:173], v[218:221], v[98:101]
	v_mfma_f32_16x16x32_bf16 v[154:157], v[166:169], v[198:201], v[154:157]
	v_mfma_f32_16x16x32_bf16 v[146:149], v[174:177], v[198:201], v[146:149]
	v_mfma_f32_16x16x32_bf16 v[138:141], v[166:169], v[206:209], v[138:141]
	v_mfma_f32_16x16x32_bf16 v[130:133], v[174:177], v[206:209], v[130:133]
	v_mfma_f32_16x16x32_bf16 v[122:125], v[166:169], v[214:217], v[122:125]
	v_mfma_f32_16x16x32_bf16 v[114:117], v[174:177], v[214:217], v[114:117]
	v_mfma_f32_16x16x32_bf16 v[106:109], v[166:169], v[222:225], v[106:109]
	v_mfma_f32_16x16x32_bf16 v[98:101], v[174:177], v[222:225], v[98:101]
	s_setprio 0
	s_barrier
	v_mov_b32_e32 v194, v232
	s_waitcnt vmcnt(2)
	s_nop 0
	v_add_u32_e32 v198, 0x10000, v194
	v_cvt_pk_bf16_f32 v194, v2, v6
	v_cvt_pk_bf16_f32 v195, v10, v14
	v_cvt_pk_bf16_f32 v196, v18, v22
	v_cvt_pk_bf16_f32 v197, v26, v30
	ds_write_b128 v198, v[194:197]
	s_nop 1
	v_cvt_pk_bf16_f32 v194, v3, v7
	v_cvt_pk_bf16_f32 v195, v11, v15
	v_cvt_pk_bf16_f32 v196, v19, v23
	v_cvt_pk_bf16_f32 v197, v27, v31
	v_xor_b32_e32 v2, 64, v198
	ds_write_b128 v2, v[194:197]
	s_nop 1
	v_cvt_pk_bf16_f32 v194, v4, v8
	v_cvt_pk_bf16_f32 v195, v12, v16
	v_cvt_pk_bf16_f32 v196, v20, v24
	v_cvt_pk_bf16_f32 v197, v28, v32
	v_xor_b32_e32 v2, 0x80, v198
	ds_write_b128 v2, v[194:197]
	s_nop 1
	v_cvt_pk_bf16_f32 v2, v5, v9
	v_cvt_pk_bf16_f32 v3, v13, v17
	v_cvt_pk_bf16_f32 v4, v21, v25
	v_cvt_pk_bf16_f32 v5, v29, v33
	v_xor_b32_e32 v6, 0xc0, v198
	ds_write_b128 v6, v[2:5]
	s_nop 1
	ds_read_b128 v[218:221], v241 offset:16384
	ds_read_b128 v[222:225], v241 offset:17408
	ds_read_b128 v[210:213], v241 offset:18432
	ds_read_b128 v[214:217], v241 offset:19456
	ds_read_b128 v[202:205], v241 offset:20480
	ds_read_b128 v[206:209], v241 offset:21504
	ds_read_b128 v[194:197], v241 offset:22528
	ds_read_b128 v[198:201], v241 offset:23552
	s_cmp_lt_u32 s54, 11
	s_cbranch_scc0 .Lpf_0
	s_add_u32 s4, s20, 0x50000
	s_addc_u32 s5, s21, 0
	v_and_b32_e32 v2, 0xff, v0
	v_lshrrev_b32_e32 v3, 2, v2
	v_and_b32_e32 v2, 3, v2
	v_lshlrev_b32_e32 v2, 7, v2
	v_lshl_or_b32 v2, v3, 10, v2
	s_mov_b32 m0, 0x20000
	s_nop 0
	global_load_lds_dword v2, s[4:5]
.Lpf_0:
	s_cmp_lt_u32 s54, 13
	s_mov_b64 s[6:7], -1
	s_cbranch_scc0 .LBB0_2253
	s_add_u32 s4, s20, 0x30000
	s_addc_u32 s5, s21, 0
	s_mov_b64 s[6:7], 0

; #define PG8_BWAIT(n) asm volatile("s_waitcnt vmcnt(" #n ")" : "+v"(bv[0]), "+v"(bv[1]), "+v"(bv[2]), "+v"(bv[3]), "+v"(bv[4]), "+v"(bv[5]), "+v"(bv[6]), "+v"(bv[7]) :: "memory")
; #define PG8_STAGE_A(bufoff, V0, V1, kb) do { \
;         __builtin_amdgcn_global_load_lds((const unsigned*)((Abase + (kb)) + (V0)), (LAS unsigned*)(lds + (bufoff) + ldsw), 16, 0, 0); \
;         __builtin_amdgcn_global_load_lds((const unsigned*)((Abase + (kb)) + (V1)), (LAS unsigned*)(lds + (bufoff) + ldsw + 8192), 16, 0, 0); } while (0)
; #define PG8_LDA(dst, b, h) do { _Pragma("unroll") for (int m = 0; m < 4; ++m) _Pragma("unroll") for (int k = 0; k < 2; ++k) dst[m][k] = *(const LAS bf16x8*)(lds + PG8_SA(b, h) + aoff + m * 2048 + k * 1024); } while (0)
; #define PG8_LDB(dst, b, h) do { _Pragma("unroll") for (int n = 0; n < 2; ++n) _Pragma("unroll") for (int k = 0; k < 2; ++k) dst[n][k] = *(const LAS bf16x8*)(lds + PG8_SB(b, h) + boff + n * 2048 + k * 1024); } while (0)
; #define PG8_MMA(ai, bj, At, Bt) do { __builtin_amdgcn_s_setprio(1); _Pragma("unroll") for (int m = 0; m < 4; ++m) _Pragma("unroll") for (int n = 0; n < 2; ++n) _Pragma("unroll") for (int k = 0; k < 2; ++k) \
;         acc[ai][bj][m][n] = __builtin_amdgcn_mfma_f32_16x16x32_bf16(Bt[n][k], At[m][k], acc[ai][bj][m][n], 0, 0, 0); __builtin_amdgcn_s_setprio(0); } while (0)
; #define PG8_WAIT_V(n) asm volatile("s_waitcnt vmcnt(" #n ")" ::: "memory")
; #define PG8_WAIT_L(n) asm volatile("s_waitcnt lgkmcnt(" #n ")" ::: "memory")
; #define PG8_BAR __builtin_amdgcn_s_barrier()
; #define PG8_SCHED __builtin_amdgcn_sched_barrier(0)
; template <class Epi, class Sched, bool ALIGN_EPI>
; __device__ __forceinline__ void gemm_phase(LAS unsigned char* lds, const Gemm g, const Sched& S, const Epi& E) {
;     ...
;             PG8_LDB(B0, 1, 0); PG8_LDB(B1, 1, 1); PG8_SCHED; PG8_LDA(At, 1, 0); PG8_STAGE_A(PG8_SA(0, 1), vc10, vc11, kb2);
;             PG8_WAIT_V(12); PG8_WAIT_L(0); PG8_BAR; PG8_MMA(0, 0, At, B0); PG8_MMA(0, 1, At, B1); PG8_BAR; PG8_SCHED;
;             PG8_BWAIT(2); PG8_BCOMMIT(1); PG8_SCHED; PG8_LDA(At, 1, 1); PG8_BISSUE(t + 4 >= nt ? pbn + (size_t)(t + 4 - nt) * 64 * Sched::LDN : pbc + (size_t)(t + 4) * 64 * Sched::LDN); PG8_STAGE_A(PG8_SA(1, 0), vc00, vc01, kb2 + 128u);
.LBB0_2257:
	v_cndmask_b32_e64 v235, v235, v245, s[6:7]
	v_cndmask_b32_e64 v234, v234, v244, s[6:7]
	s_barrier
	v_add_u32_e32 v162, 0x18000, v240
	v_add_u32_e32 v174, 0x1c000, v240
	ds_read_b128 v[178:181], v162
	ds_read_b128 v[182:185], v162 offset:1024
	ds_read_b128 v[186:189], v162 offset:2048
	ds_read_b128 v[190:193], v162 offset:3072
	ds_read_b128 v[162:165], v174
	ds_read_b128 v[166:169], v174 offset:1024
	ds_read_b128 v[170:173], v174 offset:2048
	ds_read_b128 v[174:177], v174 offset:3072
	s_mov_b32 m0, s42
	s_waitcnt lgkmcnt(0)
	ds_read_b128 v[194:197], v241 offset:32768
	ds_read_b128 v[198:201], v241 offset:33792
	ds_read_b128 v[202:205], v241 offset:34816
	ds_read_b128 v[206:209], v241 offset:35840
	ds_read_b128 v[210:213], v241 offset:36864
	ds_read_b128 v[214:217], v241 offset:37888
	ds_read_b128 v[218:221], v241 offset:38912
	ds_read_b128 v[222:225], v241 offset:39936
	global_load_lds_dwordx4 v234, s[26:27]
	s_mov_b32 m0, s43
	s_nop 0
	global_load_lds_dwordx4 v235, s[26:27]
	s_waitcnt vmcnt(12)
	s_waitcnt lgkmcnt(0)
	s_barrier
	s_setprio 1
	s_waitcnt lgkmcnt(0)
	v_mfma_f32_16x16x32_bf16 v[158:161], v[178:181], v[194:197], v[158:161]
	v_mfma_f32_16x16x32_bf16 v[150:153], v[186:189], v[194:197], v[150:153]
	v_mfma_f32_16x16x32_bf16 v[142:145], v[178:181], v[202:205], v[142:145]
	v_mfma_f32_16x16x32_bf16 v[134:137], v[186:189], v[202:205], v[134:137]
	v_mfma_f32_16x16x32_bf16 v[126:129], v[178:181], v[210:213], v[126:129]
	v_mfma_f32_16x16x32_bf16 v[118:121], v[186:189], v[210:213], v[118:121]
	v_mfma_f32_16x16x32_bf16 v[110:113], v[178:181], v[218:221], v[110:113]
	v_mfma_f32_16x16x32_bf16 v[102:105], v[186:189], v[218:221], v[102:105]
	v_mfma_f32_16x16x32_bf16 v[158:161], v[182:185], v[198:201], v[158:161]
	v_mfma_f32_16x16x32_bf16 v[150:153], v[190:193], v[198:201], v[150:153]
	v_mfma_f32_16x16x32_bf16 v[142:145], v[182:185], v[206:209], v[142:145]
	v_mfma_f32_16x16x32_bf16 v[134:137], v[190:193], v[206:209], v[134:137]
	v_mfma_f32_16x16x32_bf16 v[126:129], v[182:185], v[214:217], v[126:129]
	v_mfma_f32_16x16x32_bf16 v[118:121], v[190:193], v[214:217], v[118:121]
	v_mfma_f32_16x16x32_bf16 v[110:113], v[182:185], v[222:225], v[110:113]
	v_mfma_f32_16x16x32_bf16 v[102:105], v[190:193], v[222:225], v[102:105]
	s_setprio 0
	s_setprio 1
	v_mfma_f32_16x16x32_bf16 v[154:157], v[162:165], v[194:197], v[154:157]
	v_mfma_f32_16x16x32_bf16 v[146:149], v[170:173], v[194:197], v[146:149]
	v_mfma_f32_16x16x32_bf16 v[138:141], v[162:165], v[202:205], v[138:141]
	v_mfma_f32_16x16x32_bf16 v[130:133], v[170:173], v[202:205], v[130:133]
	v_mfma_f32_16x16x32_bf16 v[122:125], v[162:165], v[210:213], v[122:125]
	v_mfma_f32_16x16x32_bf16 v[114:117], v[170:173], v[210:213], v[114:117]
	v_mfma_f32_16x16x32_bf16 v[106:109], v[162:165], v[218:221], v[106:109]
	v_mfma_f32_16x16x32_bf16 v[98:101], v[170:173], v[218:221], v[98:101]
	v_mfma_f32_16x16x32_bf16 v[154:157], v[166:169], v[198:201], v[154:157]
	v_mfma_f32_16x16x32_bf16 v[146:149], v[174:177], v[198:201], v[146:149]
	v_mfma_f32_16x16x32_bf16 v[138:141], v[166:169], v[206:209], v[138:141]
	v_mfma_f32_16x16x32_bf16 v[130:133], v[174:177], v[206:209], v[130:133]
	v_mfma_f32_16x16x32_bf16 v[122:125], v[166:169], v[214:217], v[122:125]
	v_mfma_f32_16x16x32_bf16 v[114:117], v[174:177], v[214:217], v[114:117]
	v_mfma_f32_16x16x32_bf16 v[106:109], v[166:169], v[222:225], v[106:109]
	v_mfma_f32_16x16x32_bf16 v[98:101], v[174:177], v[222:225], v[98:101]
	s_setprio 0
	s_barrier
	v_mov_b32_e32 v194, v232
	s_waitcnt vmcnt(2)
	s_nop 0
	v_add_u32_e32 v198, 0x18000, v194
	v_cvt_pk_bf16_f32 v194, v2, v6
	v_cvt_pk_bf16_f32 v195, v10, v14
	v_cvt_pk_bf16_f32 v196, v18, v22
	v_cvt_pk_bf16_f32 v197, v26, v30
	ds_write_b128 v198, v[194:197]
	s_nop 1
	v_cvt_pk_bf16_f32 v194, v3, v7
	v_cvt_pk_bf16_f32 v195, v11, v15
	v_cvt_pk_bf16_f32 v196, v19, v23
	v_cvt_pk_bf16_f32 v197, v27, v31
	v_xor_b32_e32 v2, 64, v198
	ds_write_b128 v2, v[194:197]
	s_nop 1
	v_cvt_pk_bf16_f32 v194, v4, v8
	v_cvt_pk_bf16_f32 v195, v12, v16
	v_cvt_pk_bf16_f32 v196, v20, v24
	v_cvt_pk_bf16_f32 v197, v28, v32
	v_xor_b32_e32 v2, 0x80, v198
	ds_write_b128 v2, v[194:197]
	s_nop 1
	v_cvt_pk_bf16_f32 v2, v5, v9
	v_cvt_pk_bf16_f32 v3, v13, v17
	v_cvt_pk_bf16_f32 v4, v21, v25
	v_cvt_pk_bf16_f32 v5, v29, v33
	v_xor_b32_e32 v6, 0xc0, v198
	ds_write_b128 v6, v[2:5]
	s_nop 1
	ds_read_b128 v[218:221], v241 offset:49152
	ds_read_b128 v[222:225], v241 offset:50176
	ds_read_b128 v[210:213], v241 offset:51200
	ds_read_b128 v[214:217], v241 offset:52224
	ds_read_b128 v[202:205], v241 offset:53248
	ds_read_b128 v[206:209], v241 offset:54272
	ds_read_b128 v[194:197], v241 offset:55296
	ds_read_b128 v[198:201], v241 offset:56320
	s_cmp_lt_u32 s54, 10
	s_cbranch_scc0 .Lpf_1
	s_add_u32 s6, s20, 0x60000
	s_addc_u32 s7, s21, 0
	v_and_b32_e32 v2, 0xff, v0
	v_lshrrev_b32_e32 v3, 2, v2
	v_and_b32_e32 v2, 3, v2
	v_lshlrev_b32_e32 v2, 7, v2
	v_lshl_or_b32 v2, v3, 10, v2
	s_mov_b32 m0, 0x20000
	s_nop 0
	global_load_lds_dword v2, s[6:7]
.Lpf_1:
	s_cmp_lt_u32 s54, 12
	s_mov_b64 s[28:29], -1
	s_cbranch_scc0 .LBB0_2259
	s_add_u32 s6, s20, 0x40000
	s_addc_u32 s7, s21, 0
	s_mov_b64 s[28:29], 0

; #define PG8_BWAIT(n) asm volatile("s_waitcnt vmcnt(" #n ")" : "+v"(bv[0]), "+v"(bv[1]), "+v"(bv[2]), "+v"(bv[3]), "+v"(bv[4]), "+v"(bv[5]), "+v"(bv[6]), "+v"(bv[7]) :: "memory")
; #define PG8_STAGE_A(bufoff, V0, V1, kb) do { \
;         __builtin_amdgcn_global_load_lds((const unsigned*)((Abase + (kb)) + (V0)), (LAS unsigned*)(lds + (bufoff) + ldsw), 16, 0, 0); \
;         __builtin_amdgcn_global_load_lds((const unsigned*)((Abase + (kb)) + (V1)), (LAS unsigned*)(lds + (bufoff) + ldsw + 8192), 16, 0, 0); } while (0)
; #define PG8_LDA(dst, b, h) do { _Pragma("unroll") for (int m = 0; m < 4; ++m) _Pragma("unroll") for (int k = 0; k < 2; ++k) dst[m][k] = *(const LAS bf16x8*)(lds + PG8_SA(b, h) + aoff + m * 2048 + k * 1024); } while (0)
; #define PG8_LDB(dst, b, h) do { _Pragma("unroll") for (int n = 0; n < 2; ++n) _Pragma("unroll") for (int k = 0; k < 2; ++k) dst[n][k] = *(const LAS bf16x8*)(lds + PG8_SB(b, h) + boff + n * 2048 + k * 1024); } while (0)
; #define PG8_MMA(ai, bj, At, Bt) do { __builtin_amdgcn_s_setprio(1); _Pragma("unroll") for (int m = 0; m < 4; ++m) _Pragma("unroll") for (int n = 0; n < 2; ++n) _Pragma("unroll") for (int k = 0; k < 2; ++k) \
;         acc[ai][bj][m][n] = __builtin_amdgcn_mfma_f32_16x16x32_bf16(Bt[n][k], At[m][k], acc[ai][bj][m][n], 0, 0, 0); __builtin_amdgcn_s_setprio(0); } while (0)
; #define PG8_WAIT_V(n) asm volatile("s_waitcnt vmcnt(" #n ")" ::: "memory")
; #define PG8_WAIT_L(n) asm volatile("s_waitcnt lgkmcnt(" #n ")" ::: "memory")
; #define PG8_BAR __builtin_amdgcn_s_barrier()
; #define PG8_SCHED __builtin_amdgcn_sched_barrier(0)
; template <class Epi, class Sched, bool ALIGN_EPI>
; __device__ __forceinline__ void gemm_phase(LAS unsigned char* lds, const Gemm g, const Sched& S, const Epi& E) {
;     ...
;             PG8_LDB(B0, 0, 0); PG8_LDB(B1, 0, 1); PG8_SCHED; PG8_LDA(At, 0, 0); PG8_STAGE_A(PG8_SA(1, 1), vc10, vc11, kb1);
;             PG8_WAIT_V(12); PG8_WAIT_L(0); PG8_BAR; PG8_MMA(0, 0, At, B0); PG8_MMA(0, 1, At, B1); PG8_BAR; PG8_SCHED;
;             if (last) { vc10 = vn10; vc11 = vn11; }
;             PG8_BWAIT(2); PG8_BCOMMIT(0); PG8_SCHED; PG8_LDA(At, 0, 1); PG8_BISSUE(t + 3 >= nt ? pbn + (size_t)(t + 3 - nt) * 64 * Sched::LDN : pbc + (size_t)(t + 3) * 64 * Sched::LDN); PG8_STAGE_A(PG8_SA(0, 0), vc00, vc01, kb2);
.LBB0_4711:
	v_add_u32_e32 v162, 0x10000, v240
	v_add_u32_e32 v174, 0x14000, v240
	ds_read_b128 v[178:181], v162
	ds_read_b128 v[182:185], v162 offset:1024
	ds_read_b128 v[186:189], v162 offset:2048
	ds_read_b128 v[190:193], v162 offset:3072
	ds_read_b128 v[162:165], v174
	ds_read_b128 v[166:169], v174 offset:1024
	ds_read_b128 v[170:173], v174 offset:2048
	ds_read_b128 v[174:177], v174 offset:3072
	s_add_i32 s54, s53, 2
	s_add_i32 m0, s40, 0xc000
	s_add_u32 s2, s90, s22
	s_addc_u32 s3, s91, s23
	s_waitcnt lgkmcnt(0)
	ds_read_b128 v[194:197], v241
	ds_read_b128 v[198:201], v241 offset:1024
	ds_read_b128 v[202:205], v241 offset:2048
	ds_read_b128 v[206:209], v241 offset:3072
	ds_read_b128 v[210:213], v241 offset:4096
	ds_read_b128 v[214:217], v241 offset:5120
	ds_read_b128 v[218:221], v241 offset:6144
	ds_read_b128 v[222:225], v241 offset:7168
	global_load_lds_dwordx4 v233, s[2:3]
	s_add_i32 m0, s40, 0xe000
	s_nop 0
	global_load_lds_dwordx4 v234, s[2:3]
	s_waitcnt vmcnt(12)
	s_waitcnt lgkmcnt(0)
	s_barrier
	s_setprio 1
	s_waitcnt lgkmcnt(0)
	v_mfma_f32_16x16x32_bf16 v[158:161], v[178:181], v[194:197], v[158:161]
	v_mfma_f32_16x16x32_bf16 v[154:157], v[186:189], v[194:197], v[154:157]
	v_mfma_f32_16x16x32_bf16 v[142:145], v[178:181], v[202:205], v[142:145]
	v_mfma_f32_16x16x32_bf16 v[138:141], v[186:189], v[202:205], v[138:141]
	v_mfma_f32_16x16x32_bf16 v[126:129], v[178:181], v[210:213], v[126:129]
	v_mfma_f32_16x16x32_bf16 v[122:125], v[186:189], v[210:213], v[122:125]
	v_mfma_f32_16x16x32_bf16 v[110:113], v[178:181], v[218:221], v[110:113]
	v_mfma_f32_16x16x32_bf16 v[106:109], v[186:189], v[218:221], v[106:109]
	v_mfma_f32_16x16x32_bf16 v[158:161], v[182:185], v[198:201], v[158:161]
	v_mfma_f32_16x16x32_bf16 v[154:157], v[190:193], v[198:201], v[154:157]
	v_mfma_f32_16x16x32_bf16 v[142:145], v[182:185], v[206:209], v[142:145]
	v_mfma_f32_16x16x32_bf16 v[138:141], v[190:193], v[206:209], v[138:141]
	v_mfma_f32_16x16x32_bf16 v[126:129], v[182:185], v[214:217], v[126:129]
	v_mfma_f32_16x16x32_bf16 v[122:125], v[190:193], v[214:217], v[122:125]
	v_mfma_f32_16x16x32_bf16 v[110:113], v[182:185], v[222:225], v[110:113]
	v_mfma_f32_16x16x32_bf16 v[106:109], v[190:193], v[222:225], v[106:109]
	s_setprio 0
	s_setprio 1
	v_mfma_f32_16x16x32_bf16 v[150:153], v[162:165], v[194:197], v[150:153]
	v_mfma_f32_16x16x32_bf16 v[146:149], v[170:173], v[194:197], v[146:149]
	v_mfma_f32_16x16x32_bf16 v[134:137], v[162:165], v[202:205], v[134:137]
	v_mfma_f32_16x16x32_bf16 v[130:133], v[170:173], v[202:205], v[130:133]
	v_mfma_f32_16x16x32_bf16 v[118:121], v[162:165], v[210:213], v[118:121]
	v_mfma_f32_16x16x32_bf16 v[114:117], v[170:173], v[210:213], v[114:117]
	v_mfma_f32_16x16x32_bf16 v[102:105], v[162:165], v[218:221], v[102:105]
	v_mfma_f32_16x16x32_bf16 v[98:101], v[170:173], v[218:221], v[98:101]
	v_mfma_f32_16x16x32_bf16 v[150:153], v[166:169], v[198:201], v[150:153]
	v_mfma_f32_16x16x32_bf16 v[146:149], v[174:177], v[198:201], v[146:149]
	v_mfma_f32_16x16x32_bf16 v[134:137], v[166:169], v[206:209], v[134:137]
	v_mfma_f32_16x16x32_bf16 v[130:133], v[174:177], v[206:209], v[130:133]
	v_mfma_f32_16x16x32_bf16 v[118:121], v[166:169], v[214:217], v[118:121]
	v_mfma_f32_16x16x32_bf16 v[114:117], v[174:177], v[214:217], v[114:117]
	v_mfma_f32_16x16x32_bf16 v[102:105], v[166:169], v[222:225], v[102:105]
	v_mfma_f32_16x16x32_bf16 v[98:101], v[174:177], v[222:225], v[98:101]
	s_setprio 0
	s_barrier
	v_mov_b32_e32 v194, v235
	s_waitcnt vmcnt(2)
	s_nop 0
	v_add_u32_e32 v198, 0x10000, v194
	v_cvt_pk_bf16_f32 v194, v2, v6
	v_cvt_pk_bf16_f32 v195, v10, v14
	v_cvt_pk_bf16_f32 v196, v18, v22
	v_cvt_pk_bf16_f32 v197, v26, v30
	ds_write_b128 v198, v[194:197]
	s_nop 1
	v_cvt_pk_bf16_f32 v194, v3, v7
	v_cvt_pk_bf16_f32 v195, v11, v15
	v_cvt_pk_bf16_f32 v196, v19, v23
	v_cvt_pk_bf16_f32 v197, v27, v31
	v_xor_b32_e32 v2, 64, v198
	ds_write_b128 v2, v[194:197]
	s_nop 1
	v_cvt_pk_bf16_f32 v194, v4, v8
	v_cvt_pk_bf16_f32 v195, v12, v16
	v_cvt_pk_bf16_f32 v196, v20, v24
	v_cvt_pk_bf16_f32 v197, v28, v32
	v_xor_b32_e32 v2, 0x80, v198
	ds_write_b128 v2, v[194:197]
	s_nop 1
	v_cvt_pk_bf16_f32 v2, v5, v9
	v_cvt_pk_bf16_f32 v3, v13, v17
	v_cvt_pk_bf16_f32 v4, v21, v25
	v_cvt_pk_bf16_f32 v5, v29, v33
	v_xor_b32_e32 v6, 0xc0, v198
	ds_write_b128 v6, v[2:5]
	s_nop 1
	ds_read_b128 v[218:221], v241 offset:16384
	ds_read_b128 v[222:225], v241 offset:17408
	ds_read_b128 v[210:213], v241 offset:18432
	ds_read_b128 v[214:217], v241 offset:19456
	ds_read_b128 v[202:205], v241 offset:20480
	ds_read_b128 v[206:209], v241 offset:21504
	ds_read_b128 v[194:197], v241 offset:22528
	ds_read_b128 v[198:201], v241 offset:23552
	s_cmp_lt_u32 s54, 11
	s_cbranch_scc0 .Lpf_2
	s_add_u32 s2, s20, 0x50000
	s_addc_u32 s3, s21, 0
	v_and_b32_e32 v2, 0xff, v0
	v_lshrrev_b32_e32 v3, 2, v2
	v_and_b32_e32 v2, 3, v2
	v_lshlrev_b32_e32 v2, 7, v2
	v_lshl_or_b32 v2, v3, 10, v2
	s_mov_b32 m0, 0x20000
	s_nop 0
	global_load_lds_dword v2, s[2:3]
.Lpf_2:
	s_cmp_lt_u32 s54, 13
	s_mov_b64 s[4:5], -1
	s_cbranch_scc0 .LBB0_4713
	s_add_u32 s2, s20, 0x30000
	s_addc_u32 s3, s21, 0
	s_mov_b64 s[4:5], 0

; #define PG8_BWAIT(n) asm volatile("s_waitcnt vmcnt(" #n ")" : "+v"(bv[0]), "+v"(bv[1]), "+v"(bv[2]), "+v"(bv[3]), "+v"(bv[4]), "+v"(bv[5]), "+v"(bv[6]), "+v"(bv[7]) :: "memory")
; #define PG8_STAGE_A(bufoff, V0, V1, kb) do { \
;         __builtin_amdgcn_global_load_lds((const unsigned*)((Abase + (kb)) + (V0)), (LAS unsigned*)(lds + (bufoff) + ldsw), 16, 0, 0); \
;         __builtin_amdgcn_global_load_lds((const unsigned*)((Abase + (kb)) + (V1)), (LAS unsigned*)(lds + (bufoff) + ldsw + 8192), 16, 0, 0); } while (0)
; #define PG8_LDA(dst, b, h) do { _Pragma("unroll") for (int m = 0; m < 4; ++m) _Pragma("unroll") for (int k = 0; k < 2; ++k) dst[m][k] = *(const LAS bf16x8*)(lds + PG8_SA(b, h) + aoff + m * 2048 + k * 1024); } while (0)
; #define PG8_LDB(dst, b, h) do { _Pragma("unroll") for (int n = 0; n < 2; ++n) _Pragma("unroll") for (int k = 0; k < 2; ++k) dst[n][k] = *(const LAS bf16x8*)(lds + PG8_SB(b, h) + boff + n * 2048 + k * 1024); } while (0)
; #define PG8_MMA(ai, bj, At, Bt) do { __builtin_amdgcn_s_setprio(1); _Pragma("unroll") for (int m = 0; m < 4; ++m) _Pragma("unroll") for (int n = 0; n < 2; ++n) _Pragma("unroll") for (int k = 0; k < 2; ++k) \
;         acc[ai][bj][m][n] = __builtin_amdgcn_mfma_f32_16x16x32_bf16(Bt[n][k], At[m][k], acc[ai][bj][m][n], 0, 0, 0); __builtin_amdgcn_s_setprio(0); } while (0)
; #define PG8_WAIT_V(n) asm volatile("s_waitcnt vmcnt(" #n ")" ::: "memory")
; #define PG8_WAIT_L(n) asm volatile("s_waitcnt lgkmcnt(" #n ")" ::: "memory")
; #define PG8_BAR __builtin_amdgcn_s_barrier()
; #define PG8_SCHED __builtin_amdgcn_sched_barrier(0)
; template <class Epi, class Sched, bool ALIGN_EPI>
; __device__ __forceinline__ void gemm_phase(LAS unsigned char* lds, const Gemm g, const Sched& S, const Epi& E) {
;     ...
;             PG8_LDB(B0, 1, 0); PG8_LDB(B1, 1, 1); PG8_SCHED; PG8_LDA(At, 1, 0); PG8_STAGE_A(PG8_SA(0, 1), vc10, vc11, kb2);
;             PG8_WAIT_V(12); PG8_WAIT_L(0); PG8_BAR; PG8_MMA(0, 0, At, B0); PG8_MMA(0, 1, At, B1); PG8_BAR; PG8_SCHED;
;             PG8_BWAIT(2); PG8_BCOMMIT(1); PG8_SCHED; PG8_LDA(At, 1, 1); PG8_BISSUE(t + 4 >= nt ? pbn + (size_t)(t + 4 - nt) * 64 * Sched::LDN : pbc + (size_t)(t + 4) * 64 * Sched::LDN); PG8_STAGE_A(PG8_SA(1, 0), vc00, vc01, kb2 + 128u);
.LBB0_4717:
	v_cndmask_b32_e64 v234, v234, v245, s[4:5]
	v_cndmask_b32_e64 v233, v233, v244, s[4:5]
	s_barrier
	v_add_u32_e32 v162, 0x18000, v240
	v_add_u32_e32 v174, 0x1c000, v240
	ds_read_b128 v[178:181], v162
	ds_read_b128 v[182:185], v162 offset:1024
	ds_read_b128 v[186:189], v162 offset:2048
	ds_read_b128 v[190:193], v162 offset:3072
	ds_read_b128 v[162:165], v174
	ds_read_b128 v[166:169], v174 offset:1024
	ds_read_b128 v[170:173], v174 offset:2048
	ds_read_b128 v[174:177], v174 offset:3072
	s_mov_b32 m0, s42
	s_waitcnt lgkmcnt(0)
	ds_read_b128 v[194:197], v241 offset:32768
	ds_read_b128 v[198:201], v241 offset:33792
	ds_read_b128 v[202:205], v241 offset:34816
	ds_read_b128 v[206:209], v241 offset:35840
	ds_read_b128 v[210:213], v241 offset:36864
	ds_read_b128 v[214:217], v241 offset:37888
	ds_read_b128 v[218:221], v241 offset:38912
	ds_read_b128 v[222:225], v241 offset:39936
	global_load_lds_dwordx4 v233, s[26:27]
	s_mov_b32 m0, s43
	s_nop 0
	global_load_lds_dwordx4 v234, s[26:27]
	s_waitcnt vmcnt(12)
	s_waitcnt lgkmcnt(0)
	s_barrier
	s_setprio 1
	s_waitcnt lgkmcnt(0)
	v_mfma_f32_16x16x32_bf16 v[158:161], v[178:181], v[194:197], v[158:161]
	v_mfma_f32_16x16x32_bf16 v[154:157], v[186:189], v[194:197], v[154:157]
	v_mfma_f32_16x16x32_bf16 v[142:145], v[178:181], v[202:205], v[142:145]
	v_mfma_f32_16x16x32_bf16 v[138:141], v[186:189], v[202:205], v[138:141]
	v_mfma_f32_16x16x32_bf16 v[126:129], v[178:181], v[210:213], v[126:129]
	v_mfma_f32_16x16x32_bf16 v[122:125], v[186:189], v[210:213], v[122:125]
	v_mfma_f32_16x16x32_bf16 v[110:113], v[178:181], v[218:221], v[110:113]
	v_mfma_f32_16x16x32_bf16 v[106:109], v[186:189], v[218:221], v[106:109]
	v_mfma_f32_16x16x32_bf16 v[158:161], v[182:185], v[198:201], v[158:161]
	v_mfma_f32_16x16x32_bf16 v[154:157], v[190:193], v[198:201], v[154:157]
	v_mfma_f32_16x16x32_bf16 v[142:145], v[182:185], v[206:209], v[142:145]
	v_mfma_f32_16x16x32_bf16 v[138:141], v[190:193], v[206:209], v[138:141]
	v_mfma_f32_16x16x32_bf16 v[126:129], v[182:185], v[214:217], v[126:129]
	v_mfma_f32_16x16x32_bf16 v[122:125], v[190:193], v[214:217], v[122:125]
	v_mfma_f32_16x16x32_bf16 v[110:113], v[182:185], v[222:225], v[110:113]
	v_mfma_f32_16x16x32_bf16 v[106:109], v[190:193], v[222:225], v[106:109]
	s_setprio 0
	s_setprio 1
	v_mfma_f32_16x16x32_bf16 v[150:153], v[162:165], v[194:197], v[150:153]
	v_mfma_f32_16x16x32_bf16 v[146:149], v[170:173], v[194:197], v[146:149]
	v_mfma_f32_16x16x32_bf16 v[134:137], v[162:165], v[202:205], v[134:137]
	v_mfma_f32_16x16x32_bf16 v[130:133], v[170:173], v[202:205], v[130:133]
	v_mfma_f32_16x16x32_bf16 v[118:121], v[162:165], v[210:213], v[118:121]
	v_mfma_f32_16x16x32_bf16 v[114:117], v[170:173], v[210:213], v[114:117]
	v_mfma_f32_16x16x32_bf16 v[102:105], v[162:165], v[218:221], v[102:105]
	v_mfma_f32_16x16x32_bf16 v[98:101], v[170:173], v[218:221], v[98:101]
	v_mfma_f32_16x16x32_bf16 v[150:153], v[166:169], v[198:201], v[150:153]
	v_mfma_f32_16x16x32_bf16 v[146:149], v[174:177], v[198:201], v[146:149]
	v_mfma_f32_16x16x32_bf16 v[134:137], v[166:169], v[206:209], v[134:137]
	v_mfma_f32_16x16x32_bf16 v[130:133], v[174:177], v[206:209], v[130:133]
	v_mfma_f32_16x16x32_bf16 v[118:121], v[166:169], v[214:217], v[118:121]
	v_mfma_f32_16x16x32_bf16 v[114:117], v[174:177], v[214:217], v[114:117]
	v_mfma_f32_16x16x32_bf16 v[102:105], v[166:169], v[222:225], v[102:105]
	v_mfma_f32_16x16x32_bf16 v[98:101], v[174:177], v[222:225], v[98:101]
	s_setprio 0
	s_barrier
	v_mov_b32_e32 v194, v235
	s_waitcnt vmcnt(2)
	s_nop 0
	v_add_u32_e32 v198, 0x18000, v194
	v_cvt_pk_bf16_f32 v194, v2, v6
	v_cvt_pk_bf16_f32 v195, v10, v14
	v_cvt_pk_bf16_f32 v196, v18, v22
	v_cvt_pk_bf16_f32 v197, v26, v30
	ds_write_b128 v198, v[194:197]
	s_nop 1
	v_cvt_pk_bf16_f32 v194, v3, v7
	v_cvt_pk_bf16_f32 v195, v11, v15
	v_cvt_pk_bf16_f32 v196, v19, v23
	v_cvt_pk_bf16_f32 v197, v27, v31
	v_xor_b32_e32 v2, 64, v198
	ds_write_b128 v2, v[194:197]
	s_nop 1
	v_cvt_pk_bf16_f32 v194, v4, v8
	v_cvt_pk_bf16_f32 v195, v12, v16
	v_cvt_pk_bf16_f32 v196, v20, v24
	v_cvt_pk_bf16_f32 v197, v28, v32
	v_xor_b32_e32 v2, 0x80, v198
	ds_write_b128 v2, v[194:197]
	s_nop 1
	v_cvt_pk_bf16_f32 v2, v5, v9
	v_cvt_pk_bf16_f32 v3, v13, v17
	v_cvt_pk_bf16_f32 v4, v21, v25
	v_cvt_pk_bf16_f32 v5, v29, v33
	v_xor_b32_e32 v6, 0xc0, v198
	ds_write_b128 v6, v[2:5]
	s_nop 1
	ds_read_b128 v[218:221], v241 offset:49152
	ds_read_b128 v[222:225], v241 offset:50176
	ds_read_b128 v[210:213], v241 offset:51200
	ds_read_b128 v[214:217], v241 offset:52224
	ds_read_b128 v[202:205], v241 offset:53248
	ds_read_b128 v[206:209], v241 offset:54272
	ds_read_b128 v[194:197], v241 offset:55296
	ds_read_b128 v[198:201], v241 offset:56320
	s_cmp_lt_u32 s54, 10
	s_cbranch_scc0 .Lpf_3
	s_add_u32 s4, s20, 0x60000
	s_addc_u32 s5, s21, 0
	v_and_b32_e32 v2, 0xff, v0
	v_lshrrev_b32_e32 v3, 2, v2
	v_and_b32_e32 v2, 3, v2
	v_lshlrev_b32_e32 v2, 7, v2
	v_lshl_or_b32 v2, v3, 10, v2
	s_mov_b32 m0, 0x20000
	s_nop 0
	global_load_lds_dword v2, s[4:5]
.Lpf_3:
	s_cmp_lt_u32 s54, 12
	s_mov_b64 s[28:29], -1
	s_cbranch_scc0 .LBB0_4719
	s_add_u32 s4, s20, 0x40000
	s_addc_u32 s5, s21, 0
	s_mov_b64 s[28:29], 0
